# v35 + final phase: final-norm gain loaded once before the row loop; the per-piece load->vmcnt(0)->store chain no longer drains every output store (8 store round trips per row removed)
# speedup vs baseline: 1.0094x; 1.0039x over previous
; #define GAS __attribute__((address_space(1)))
; __device__ __forceinline__ void final_phase(Frame& F) {
;     const bf16* Y2 = WSP(const bf16, WS_Z); const float* mod = WSP(const float, WS_MOD1); const float* fg = F.in[34];
;     const int* tok_e = WSP(const int, WS_ROUTE); const int* tok_rank = tok_e + 2 * ML; const float* tok_w = (const float*)(tok_rank + 2 * ML);
;     int off[8]; { int t = 0;
; #pragma unroll
;         for (int e = 0; e < 8; ++e) { off[e] = t; t += ((__builtin_amdgcn_readfirstlane((int)F.ctl[CW_CNT + e]) + 255) >> 8) << 8; } }
;     const int gw = F.vcu * NWAVES + F.wave, NGW = F.G * NWAVES;
;     for (int row = gw; row < ML; row += NGW) {
;         const int e0 = tok_e[2 * row], e1 = tok_e[2 * row + 1]; int o0 = 0, o1 = 0;
; #pragma unroll
;         for (int k = 0; k < 8; ++k) { o0 = (e0 == k) ? off[k] : o0; o1 = (e1 == k) ? off[k] : o1; }
;         const size_t s0 = (size_t)(o0 + tok_rank[2 * row]) * DM, s1 = (size_t)(o1 + tok_rank[2 * row + 1]) * DM; const float w0 = tok_w[2 * row], w1 = tok_w[2 * row + 1];
;         const float* g2 = mod + (size_t)(row >> 13) * MOD_W + 5 * DM;
;         GAS f32x4* xr = (GAS f32x4*)(F.out + (size_t)row * DM) + F.lane;
.LBB0_2186:
	s_cmp_lt_i32 s90, 20
	s_cselect_b64 s[2:3], -1, 0
	s_and_b64 s[0:1], s[2:3], s[0:1]
	s_andn2_b64 vcc, exec, s[0:1]
	s_cbranch_vccnz .LBB0_2258
	s_add_u32 s0, s88, 0x8000
	v_mov_b32_e32 v0, 0x8000
	s_waitcnt vmcnt(0)
	v_mov_b32_e32 v29, 0
	s_addc_u32 s1, s89, 0
	global_load_dwordx4 v[0:3], v0, s[88:89]
	s_nop 0
	global_load_dwordx3 v[4:6], v29, s[0:1] offset:16
	s_lshl_b32 s0, s92, 3
	s_add_i32 s6, s0, s94
	s_cmpk_gt_i32 s6, 0x3fff
	s_waitcnt vmcnt(0)
	v_readfirstlane_b32 s7, v0
	v_readfirstlane_b32 s5, v1
	v_readfirstlane_b32 s4, v2
	v_readfirstlane_b32 s3, v3
	v_readfirstlane_b32 s2, v4
	v_readfirstlane_b32 s1, v5
	v_readfirstlane_b32 s0, v6
	s_cbranch_scc1 .LBB0_2258
	v_mbcnt_lo_u32_b32 v0, -1, 0
	v_mbcnt_hi_u32_b32 v0, -1, v0
	v_and_b32_e32 v1, 64, v0
	v_add_u32_e32 v1, 64, v1
	v_xor_b32_e32 v2, 1, v0
	v_cmp_lt_i32_e32 vcc, v2, v1
	s_add_u32 s28, s88, 0x220000
	s_addc_u32 s29, s89, 0
	v_cndmask_b32_e32 v2, v0, v2, vcc
	s_addk_i32 s7, 0xff
	s_addk_i32 s5, 0xff
	v_lshlrev_b32_e32 v31, 2, v2
	v_xor_b32_e32 v2, 2, v0
	s_and_b32 s30, s7, 0xffffff00
	s_and_b32 s31, s5, 0xffffff00
	s_addk_i32 s4, 0xff
	v_cmp_lt_i32_e32 vcc, v2, v1
	s_add_i32 s31, s31, s30
	s_and_b32 s33, s4, 0xffffff00
	s_addk_i32 s3, 0xff
	v_cndmask_b32_e32 v2, v0, v2, vcc
	s_add_i32 s33, s33, s31
	s_and_b32 s34, s3, 0xffffff00
	s_addk_i32 s2, 0xff
	s_waitcnt lgkmcnt(0)
	v_lshlrev_b32_e32 v35, 2, v2
	v_xor_b32_e32 v2, 4, v0
	s_add_i32 s34, s34, s33
	s_and_b32 s35, s2, 0xffffff00
	s_addk_i32 s1, 0xff
	v_cmp_lt_i32_e32 vcc, v2, v1
	s_add_i32 s35, s35, s34
	s_and_b32 s36, s1, 0xffffff00
	s_addk_i32 s0, 0xff
	v_cndmask_b32_e32 v2, v0, v2, vcc
	s_add_i32 s36, s36, s35
	s_and_b32 s37, s0, 0xffffff00
	v_lshlrev_b32_e32 v37, 2, v2
	v_xor_b32_e32 v2, 8, v0
	s_add_i32 s37, s37, s36
	v_cmp_lt_i32_e32 vcc, v2, v1
	s_add_u32 s8, s88, 0x26700000
	s_addc_u32 s9, s89, 0
	v_cndmask_b32_e32 v2, v0, v2, vcc
	v_lshlrev_b32_e32 v39, 2, v2
	v_xor_b32_e32 v2, 16, v0
	s_add_u32 s38, s88, 0x200000
	v_cmp_lt_i32_e32 vcc, v2, v1
	s_addc_u32 s39, s89, 0
	s_add_u32 s40, s88, 0x240000
	v_cndmask_b32_e32 v2, v0, v2, vcc
	v_lshlrev_b32_e32 v41, 2, v2
	v_xor_b32_e32 v2, 32, v0
	s_addc_u32 s41, s89, 0
	s_lshl_b32 s10, s93, 3
	v_cmp_lt_i32_e32 vcc, v2, v1
	v_lshlrev_b32_e32 v30, 2, v178
	v_readlane_b32 s12, v250, 0
	v_cndmask_b32_e32 v0, v0, v2, vcc
	v_readlane_b32 s13, v250, 1
	v_readlane_b32 s14, v250, 2
	v_readlane_b32 s15, v250, 3
	v_readlane_b32 s16, v250, 4
	v_readlane_b32 s17, v250, 5
	v_or_b32_e32 v44, 0x500, v30
	s_add_u32 s42, s88, 0x15a00000
	v_lshlrev_b32_e32 v45, 2, v0
	v_readlane_b32 s18, v250, 6
	v_readlane_b32 s19, v250, 7
	s_mov_b64 s[12:13], s[16:17]
	v_lshlrev_b32_e32 v0, 2, v44
	v_mov_b32_e32 v1, v29
	v_or_b32_e32 v48, 0x600, v30
	s_addc_u32 s43, s89, 0
	s_ashr_i32 s7, s6, 31
	v_lshl_add_u64 v[46:47], s[12:13], 0, v[0:1]
	v_lshlrev_b32_e32 v0, 2, v48
	v_or_b32_e32 v52, 0x700, v30
	s_lshl_b64 s[2:3], s[6:7], 12
	v_lshl_add_u64 v[50:51], s[12:13], 0, v[0:1]
	v_lshlrev_b32_e32 v0, 2, v52
	s_add_u32 s2, s88, s2
	v_lshl_add_u64 v[54:55], s[12:13], 0, v[0:1]
	v_lshlrev_b32_e32 v0, 3, v178
	s_addc_u32 s3, s89, s3
	v_lshlrev_b32_e32 v28, 4, v178
	v_lshl_add_u64 v[56:57], s[8:9], 0, v[0:1]
	v_lshl_add_u64 v[0:1], s[2:3], 0, v[0:1]
	s_mov_b64 s[2:3], 0x4d800000
	s_ashr_i32 s11, s10, 31
	s_mov_b64 s[14:15], s[18:19]
	v_lshl_add_u64 v[32:33], s[12:13], 0, v[28:29]
	v_lshl_add_u64 v[58:59], v[0:1], 0, s[2:3]
	s_lshl_b64 s[12:13], s[10:11], 12
	s_lshl_b64 s[2:3], s[6:7], 13
	s_add_u32 s2, s14, s2
	s_addc_u32 s3, s15, s3
	s_mov_b64 s[0:1], 0x1000
	v_lshl_add_u64 v[0:1], s[2:3], 0, v[28:29]
	v_lshl_add_u64 v[42:43], v[32:33], 0, s[0:1]
	v_lshl_add_u64 v[60:61], v[0:1], 0, s[0:1]
	s_lshl_b32 s0, s92, 4
	s_lshl_b32 s1, s94, 1
	v_or_b32_e32 v34, 0x100, v30
	v_or_b32_e32 v36, 0x200, v30
	v_or_b32_e32 v38, 0x300, v30
	v_or_b32_e32 v40, 0x400, v30
	s_lshl_b64 s[14:15], s[10:11], 13
	s_add_i32 s16, s0, s1
	s_lshl_b32 s7, s93, 4
	v_mov_b32_e32 v49, 0x358637bd
	s_mov_b32 s11, 0xf800000
	v_mov_b32_e32 v53, 0x260
	v_mov_b64_e32 v[62:63], 0x3ffffff
	global_load_dwordx4 v[200:203], v[32:33], off
	global_load_dwordx4 v[204:207], v[32:33], off offset:1024
	global_load_dwordx4 v[208:211], v[32:33], off offset:2048
	global_load_dwordx4 v[212:215], v[32:33], off offset:3072
	global_load_dwordx4 v[216:219], v[42:43], off
	global_load_dwordx4 v[220:223], v[46:47], off
	global_load_dwordx4 v[224:227], v[50:51], off
	global_load_dwordx4 v[228:231], v[54:55], off
	s_branch .LBB0_2191

; #define GAS __attribute__((address_space(1)))
; __device__ __forceinline__ void final_phase(Frame& F) {
;     ...
;         const float rstd = 1.0f / sqrtf(wave_sum(s) * (1.0f / DM) + NORM_EPS);
; #pragma unroll
;         for (int j = 0; j < 8; ++j) { const int col = 4 * (F.lane + 64 * j); xr[64 * j] = v[j] * rstd * *(const GAS f32x4*)(fg + col); }
.LBB0_2190:
	s_waitcnt vmcnt(2)
	v_mul_f32_e32 v64, v5, v5
	v_mul_f32_e32 v65, v7, v7
	v_fmac_f32_e32 v64, v4, v4
	v_fmac_f32_e32 v65, v6, v6
	v_add_f32_e32 v64, v64, v65
	v_add_f32_e32 v28, v28, v64
	ds_bpermute_b32 v64, v31, v28
	s_add_i32 s6, s6, s10
	s_add_i32 s16, s16, s7
	v_lshl_add_u64 v[58:59], v[58:59], 0, s[12:13]
	s_cmpk_lt_i32 s6, 0x4000
	s_waitcnt lgkmcnt(0)
	v_add_f32_e32 v28, v28, v64
	ds_bpermute_b32 v64, v35, v28
	s_waitcnt lgkmcnt(0)
	v_add_f32_e32 v28, v28, v64
	ds_bpermute_b32 v64, v37, v28
	s_waitcnt lgkmcnt(0)
	v_add_f32_e32 v28, v28, v64
	ds_bpermute_b32 v64, v39, v28
	s_waitcnt lgkmcnt(0)
	v_add_f32_e32 v28, v28, v64
	ds_bpermute_b32 v64, v41, v28
	s_waitcnt lgkmcnt(0)
	v_add_f32_e32 v28, v28, v64
	ds_bpermute_b32 v64, v45, v28
	s_waitcnt lgkmcnt(0)
	v_add_f32_e32 v28, v28, v64
	v_fmamk_f32 v28, v28, 0x3a000000, v49
	v_mul_f32_e32 v64, 0x4f800000, v28
	v_cmp_gt_f32_e32 vcc, s11, v28
	s_nop 1
	v_cndmask_b32_e32 v28, v28, v64, vcc
	v_sqrt_f32_e32 v64, v28
	s_nop 0
	v_add_u32_e32 v65, -1, v64
	s_waitcnt vmcnt(1)
	v_add_u32_e32 v66, 1, v64
	v_fma_f32 v67, -v65, v64, v28
	v_fma_f32 v76, -v66, v64, v28
	v_cmp_ge_f32_e64 s[0:1], 0, v67
	s_nop 1
	v_cndmask_b32_e64 v64, v64, v65, s[0:1]
	v_cmp_lt_f32_e64 s[0:1], 0, v76
	s_nop 1
	v_cndmask_b32_e64 v64, v64, v66, s[0:1]
	v_mul_f32_e32 v65, 0x37800000, v64
	v_cndmask_b32_e32 v64, v64, v65, vcc
	v_cmp_class_f32_e32 vcc, v28, v53
	s_nop 1
	v_cndmask_b32_e32 v28, v64, v28, vcc
	v_div_scale_f32 v64, s[0:1], v28, v28, 1.0
	v_rcp_f32_e32 v65, v64
	v_div_scale_f32 v66, vcc, 1.0, v28, 1.0
	v_fma_f32 v67, -v64, v65, 1.0
	v_fmac_f32_e32 v65, v67, v65
	v_mul_f32_e32 v67, v66, v65
	v_fma_f32 v76, -v64, v67, v66
	v_fmac_f32_e32 v67, v76, v65
	v_fma_f32 v64, -v64, v67, v66
	v_div_fmas_f32 v64, v64, v65, v67
	v_div_fixup_f32 v28, v64, v28, 1.0
	v_pk_mul_f32 v[64:65], v[70:71], v[28:29] op_sel_hi:[1,0]
	v_pk_mul_f32 v[66:67], v[68:69], v[28:29] op_sel_hi:[1,0]
	s_waitcnt vmcnt(0)
	v_pk_mul_f32 v[24:25], v[200:201], v[64:65]
	v_pk_mul_f32 v[26:27], v[202:203], v[66:67]
	global_store_dwordx4 v[60:61], v[24:27], off offset:-4096
	s_nop 1
	v_pk_mul_f32 v[64:65], v[72:73], v[28:29] op_sel_hi:[1,0]
	v_pk_mul_f32 v[66:67], v[74:75], v[28:29] op_sel_hi:[1,0]
	v_pk_mul_f32 v[10:11], v[10:11], v[28:29] op_sel_hi:[1,0]
	v_pk_mul_f32 v[8:9], v[8:9], v[28:29] op_sel_hi:[1,0]
	v_pk_mul_f32 v[14:15], v[14:15], v[28:29] op_sel_hi:[1,0]
	v_pk_mul_f32 v[12:13], v[12:13], v[28:29] op_sel_hi:[1,0]
	v_pk_mul_f32 v[2:3], v[2:3], v[28:29] op_sel_hi:[1,0]
	v_pk_mul_f32 v[0:1], v[0:1], v[28:29] op_sel_hi:[1,0]
	v_pk_mul_f32 v[6:7], v[6:7], v[28:29] op_sel_hi:[1,0]
	v_pk_mul_f32 v[4:5], v[4:5], v[28:29] op_sel_hi:[1,0]
	v_pk_mul_f32 v[24:25], v[204:205], v[66:67]
	v_pk_mul_f32 v[26:27], v[206:207], v[64:65]
	global_store_dwordx4 v[60:61], v[24:27], off offset:-3072
	s_nop 1
	v_pk_mul_f32 v[8:9], v[208:209], v[8:9]
	v_pk_mul_f32 v[10:11], v[210:211], v[10:11]
	global_store_dwordx4 v[60:61], v[8:11], off offset:-2048
	s_nop 1
	v_pk_mul_f32 v[8:9], v[212:213], v[12:13]
	v_pk_mul_f32 v[10:11], v[214:215], v[14:15]
	global_store_dwordx4 v[60:61], v[8:11], off offset:-1024
	s_nop 1
	v_pk_mul_f32 v[12:13], v[18:19], v[28:29] op_sel_hi:[1,0]
	v_pk_mul_f32 v[14:15], v[16:17], v[28:29] op_sel_hi:[1,0]
	v_pk_mul_f32 v[10:11], v[12:13], v[218:219]
	v_pk_mul_f32 v[8:9], v[14:15], v[216:217]
	global_store_dwordx4 v[60:61], v[8:11], off
	s_nop 1
	v_pk_mul_f32 v[12:13], v[22:23], v[28:29] op_sel_hi:[1,0]
	v_pk_mul_f32 v[14:15], v[20:21], v[28:29] op_sel_hi:[1,0]
	v_pk_mul_f32 v[10:11], v[12:13], v[222:223]
	v_pk_mul_f32 v[8:9], v[14:15], v[220:221]
	global_store_dwordx4 v[60:61], v[8:11], off offset:1024
	s_nop 1
	v_pk_mul_f32 v[0:1], v[0:1], v[224:225]
	v_pk_mul_f32 v[2:3], v[2:3], v[226:227]
	global_store_dwordx4 v[60:61], v[0:3], off offset:2048
	s_nop 1
	v_pk_mul_f32 v[0:1], v[4:5], v[228:229]
	v_pk_mul_f32 v[2:3], v[6:7], v[230:231]
	global_store_dwordx4 v[60:61], v[0:3], off offset:3072
	s_nop 1
	v_lshl_add_u64 v[60:61], v[60:61], 0, s[14:15]
	s_cbranch_scc0 .LBB0_2258
